# grid barrier: the acquire-side buffer_inv issued at arrival (after the workgroup has drained its loads, right behind the arrive atomic) instead of after the release is observed
# speedup vs baseline: 1.0093x; 1.0086x over previous
.LBB0_184:
	s_mov_b64 s[6:7], exec
	s_lshl_b32 s2, s33, 8
	v_readlane_b32 s4, v252, 19
	v_mbcnt_lo_u32_b32 v1, s6, 0
	v_readlane_b32 s5, v252, 20
	s_add_u32 s4, s4, s2
	v_mbcnt_hi_u32_b32 v1, s7, v1
	s_mov_b32 s3, 0
	s_addc_u32 s5, s5, 0
	v_cmp_eq_u32_e32 vcc, 0, v1
	s_and_saveexec_b64 s[8:9], vcc
	s_cbranch_execz .LBB0_186
	s_bcnt1_i32_b64 s2, s[6:7]
	v_mov_b32_e32 v3, 0x1000
	v_mov_b32_e32 v4, s2
	global_atomic_add v3, v3, v4, s[4:5] offset:1024 sc0
	buffer_inv sc1
.LBB0_186:
	s_or_b64 exec, exec, s[8:9]
	v_cvt_f32_u32_e32 v4, v2
	s_waitcnt vmcnt(1)
	v_readfirstlane_b32 s6, v3
	v_sub_u32_e32 v3, 0, v2
	s_lshl_b32 s2, s33, 6
	v_rcp_iflag_f32_e32 v4, v4
	v_add_u32_e32 v5, s6, v1
	v_mul_f32_e32 v4, 0x4f7ffffe, v4
	v_cvt_u32_f32_e32 v4, v4
	v_mul_lo_u32 v1, v3, v4
	v_mul_hi_u32 v1, v4, v1
	v_add_u32_e32 v1, v4, v1
	v_mul_hi_u32 v1, v5, v1
	v_mul_lo_u32 v3, v1, v2
	v_sub_u32_e32 v3, v5, v3
	v_add_u32_e32 v4, 1, v1
	v_cmp_ge_u32_e32 vcc, v3, v2
	s_nop 1
	v_cndmask_b32_e32 v1, v1, v4, vcc
	v_sub_u32_e32 v4, v3, v2
	v_cndmask_b32_e32 v3, v3, v4, vcc
	v_add_u32_e32 v4, 1, v1
	v_cmp_ge_u32_e32 vcc, v3, v2
	v_add_u32_e32 v3, 1, v5
	s_nop 0
	v_cndmask_b32_e32 v1, v1, v4, vcc
	v_mul_lo_u32 v4, v2, v1
	v_add_u32_e32 v2, v4, v2
	v_cmp_ne_u32_e32 vcc, v3, v2
	s_and_saveexec_b64 s[6:7], vcc
	s_xor_b64 s[6:7], exec, s[6:7]
	s_cbranch_execz .LBB0_200
	s_waitcnt lgkmcnt(0)
	v_mov_b32_e32 v0, 0x2000
	global_load_dword v0, v0, s[4:5] offset:1024 sc1
	s_add_u32 s14, s4, 0x2400
	s_addc_u32 s15, s5, 0
	s_waitcnt vmcnt(0)
	v_cmp_eq_u32_e32 vcc, v0, v1
	s_and_saveexec_b64 s[8:9], vcc
	s_cbranch_execz .LBB0_199
	s_add_u32 s10, s70, 0x4200
	s_addc_u32 s11, s71, 0
	s_mov_b32 s26, 1
	s_mov_b64 s[16:17], 0
	v_mov_b32_e32 v0, 0
	s_branch .LBB0_190

.LBB0_199:
	s_or_b64 exec, exec, s[8:9]
	s_waitcnt vmcnt(0)
	s_nop 0
	s_waitcnt vmcnt(0)

.LBB0_217:
	s_or_b64 exec, exec, s[8:9]
	s_mov_b64 s[8:9], exec
	v_mbcnt_lo_u32_b32 v0, s8, 0
	v_mbcnt_hi_u32_b32 v0, s9, v0
	v_cmp_eq_u32_e32 vcc, 0, v0
	s_waitcnt vmcnt(0)
	s_nop 0
	s_and_saveexec_b64 s[10:11], vcc
	s_cbranch_execz .LBB0_219
	s_bcnt1_i32_b64 s8, s[8:9]
	v_mov_b32_e32 v0, 0x2000
	v_mov_b32_e32 v1, s8
	global_atomic_add v0, v1, s[4:5] offset:1024

.LBB0_222:
	s_or_b64 exec, exec, s[2:3]
	s_waitcnt vmcnt(0)
	global_atomic_add v[170:171], v187, off
	s_nop 0
	s_waitcnt vmcnt(0)

.LBB0_476:
	global_atomic_add v3, v[168:169], v187, off sc0
	buffer_inv sc1
	v_cvt_f32_u32_e32 v1, v2
	v_sub_u32_e32 v4, 0, v2
	v_rcp_iflag_f32_e32 v1, v1
	s_nop 0
	v_mul_f32_e32 v1, 0x4f7ffffe, v1
	v_cvt_u32_f32_e32 v1, v1
	v_mul_lo_u32 v4, v4, v1
	v_mul_hi_u32 v4, v1, v4
	v_add_u32_e32 v1, v1, v4
	s_waitcnt vmcnt(1)
	v_mul_hi_u32 v1, v3, v1
	v_mul_lo_u32 v4, v1, v2
	v_sub_u32_e32 v4, v3, v4
	v_add_u32_e32 v5, 1, v1
	v_cmp_ge_u32_e32 vcc, v4, v2
	v_add_u32_e32 v3, 1, v3
	s_nop 0
	v_cndmask_b32_e32 v1, v1, v5, vcc
	v_sub_u32_e32 v5, v4, v2
	v_cndmask_b32_e32 v4, v4, v5, vcc
	v_add_u32_e32 v5, 1, v1
	v_cmp_ge_u32_e32 vcc, v4, v2
	s_nop 1
	v_cndmask_b32_e32 v1, v1, v5, vcc
	v_mul_lo_u32 v4, v2, v1
	v_add_u32_e32 v2, v4, v2
	v_cmp_ne_u32_e32 vcc, v3, v2
	s_and_saveexec_b64 s[2:3], vcc
	s_xor_b64 s[2:3], exec, s[2:3]
	s_cbranch_execz .LBB0_490
	s_waitcnt lgkmcnt(0)
	global_load_dword v0, v[170:171], off sc1
	s_waitcnt vmcnt(0)
	v_cmp_eq_u32_e32 vcc, v0, v1
	s_and_saveexec_b64 s[4:5], vcc
	s_cbranch_execz .LBB0_489
	s_mov_b32 s7, 1
	s_mov_b64 s[8:9], 0
	s_branch .LBB0_480

.LBB0_489:
	s_or_b64 exec, exec, s[4:5]
	s_waitcnt vmcnt(0)
	s_nop 0
	s_waitcnt vmcnt(0)

.LBB0_853:
	global_atomic_add v3, v[168:169], v187, off sc0
	buffer_inv sc1
	v_cvt_f32_u32_e32 v1, v2
	v_sub_u32_e32 v4, 0, v2
	v_rcp_iflag_f32_e32 v1, v1
	s_nop 0
	v_mul_f32_e32 v1, 0x4f7ffffe, v1
	v_cvt_u32_f32_e32 v1, v1
	v_mul_lo_u32 v4, v4, v1
	v_mul_hi_u32 v4, v1, v4
	v_add_u32_e32 v1, v1, v4
	s_waitcnt vmcnt(1)
	v_mul_hi_u32 v1, v3, v1
	v_mul_lo_u32 v4, v1, v2
	v_sub_u32_e32 v4, v3, v4
	v_add_u32_e32 v5, 1, v1
	v_cmp_ge_u32_e32 vcc, v4, v2
	v_add_u32_e32 v3, 1, v3
	s_nop 0
	v_cndmask_b32_e32 v1, v1, v5, vcc
	v_sub_u32_e32 v5, v4, v2
	v_cndmask_b32_e32 v4, v4, v5, vcc
	v_add_u32_e32 v5, 1, v1
	v_cmp_ge_u32_e32 vcc, v4, v2
	s_nop 1
	v_cndmask_b32_e32 v1, v1, v5, vcc
	v_mul_lo_u32 v4, v2, v1
	v_add_u32_e32 v2, v4, v2
	v_cmp_ne_u32_e32 vcc, v3, v2
	s_and_saveexec_b64 s[2:3], vcc
	s_xor_b64 s[2:3], exec, s[2:3]
	s_cbranch_execz .LBB0_867
	s_waitcnt lgkmcnt(0)
	global_load_dword v0, v[170:171], off sc1
	s_waitcnt vmcnt(0)
	v_cmp_eq_u32_e32 vcc, v0, v1
	s_and_saveexec_b64 s[8:9], vcc
	s_cbranch_execz .LBB0_866
	s_mov_b32 s12, 1
	s_mov_b64 s[10:11], 0
	s_branch .LBB0_857

.LBB0_1197:
	global_atomic_add v3, v[168:169], v187, off sc0
	buffer_inv sc1
	v_cvt_f32_u32_e32 v1, v2
	v_sub_u32_e32 v4, 0, v2
	v_rcp_iflag_f32_e32 v1, v1
	s_nop 0
	v_mul_f32_e32 v1, 0x4f7ffffe, v1
	v_cvt_u32_f32_e32 v1, v1
	v_mul_lo_u32 v4, v4, v1
	v_mul_hi_u32 v4, v1, v4
	v_add_u32_e32 v1, v1, v4
	s_waitcnt vmcnt(1)
	v_mul_hi_u32 v1, v3, v1
	v_mul_lo_u32 v4, v1, v2
	v_sub_u32_e32 v4, v3, v4
	v_add_u32_e32 v5, 1, v1
	v_cmp_ge_u32_e32 vcc, v4, v2
	v_add_u32_e32 v3, 1, v3
	s_nop 0
	v_cndmask_b32_e32 v1, v1, v5, vcc
	v_sub_u32_e32 v5, v4, v2
	v_cndmask_b32_e32 v4, v4, v5, vcc
	v_add_u32_e32 v5, 1, v1
	v_cmp_ge_u32_e32 vcc, v4, v2
	s_nop 1
	v_cndmask_b32_e32 v1, v1, v5, vcc
	v_mul_lo_u32 v4, v2, v1
	v_add_u32_e32 v2, v4, v2
	v_cmp_ne_u32_e32 vcc, v3, v2
	s_and_saveexec_b64 s[2:3], vcc
	s_xor_b64 s[2:3], exec, s[2:3]
	s_cbranch_execz .LBB0_1211
	s_waitcnt lgkmcnt(0)
	global_load_dword v0, v[170:171], off sc1
	s_waitcnt vmcnt(0)
	v_cmp_eq_u32_e32 vcc, v0, v1
	s_and_saveexec_b64 s[8:9], vcc
	s_cbranch_execz .LBB0_1210
	s_mov_b32 s7, 1
	s_mov_b64 s[10:11], 0
	s_branch .LBB0_1201
